# speedup vs baseline: 1.0057x; 1.0057x over previous
_Z6k_gemmPKfS0_PK15HIP_vector_typeIjLj4EEPDF16_PKh:
	s_load_dwordx4 s[20:23], s[0:1], 0x0
	s_load_dwordx4 s[4:7], s[0:1], 0x10
	s_load_dwordx2 s[38:39], s[0:1], 0x20
	v_readfirstlane_b32 s8, v0
	v_and_b32_e32 v1, 63, v0
	s_nop 3
	s_lshr_b32 s8, s8, 6
	s_and_b32 s40, s2, 7
	s_lshr_b32 s41, s2, 3
	s_mul_i32 s18, s40, 0x187
	s_add_u32 s19, s18, 0x187
	s_min_u32 s19, s19, 0xc35
	s_sub_u32 s33, s19, s18
	s_sub_u32 s33, s33, 0x180
	s_lshl_b32 s33, s33, 2
	s_cmp_lt_u32 s41, s33
	s_cselect_b32 s44, 7, 6
	s_lshr_b32 s45, s41, 2
	s_add_u32 s45, s45, s18
	s_add_u32 s45, s45, 0x180
	s_lshl_b32 s45, s45, 4
	s_and_b32 s46, s41, 3
	s_lshl_b32 s46, s46, 2
	s_add_u32 s47, s45, s46
	s_mul_i32 s45, s47, 0x4b0
	s_lshl_b32 s46, s47, 8
	s_add_i32 s18, s18, s41
	s_cmp_eq_u32 s8, 0
	s_cselect_b32 s9, s44, 6
	s_add_i32 s11, s44, 4
	s_lshl_b32 s18, s18, 4
	s_lshl_b32 s19, s8, 2
	s_add_i32 s33, s18, s19
	s_mul_i32 s12, s33, 0x4b0
	s_lshl_b32 s32, s18, 8
	s_sub_u32 s32, s32, 0x100000
	s_mov_b32 s10, 0
	v_lshl_add_u32 v253, v1, 10, s33
	v_mov_b32_e32 v254, s47
	v_cmp_eq_u32_e32 vcc, 6, v1
	s_nop 1
	v_cndmask_b32_e32 v253, v253, v254, vcc
	v_mov_b32_e32 v247, 0
	v_cmp_gt_i32_e32 vcc, s9, v1
	s_mov_b32 s18, 0xc350
	v_cmp_gt_i32_e64 s[36:37], s18, v253
	s_and_b64 vcc, vcc, s[36:37]
	s_waitcnt lgkmcnt(0)
	s_and_saveexec_b64 s[36:37], vcc
	global_load_dword v247, v253, s[38:39]
	s_mov_b64 exec, s[36:37]
	s_mov_b32 s24, s22
	s_and_b32 s25, s23, 0xffff
	s_mov_b32 s26, 0x3938700
	s_mov_b32 s27, 0x20000
	s_and_b32 s21, s21, 0xffff
	s_mov_b32 s22, 0x3938700
	s_mov_b32 s23, 0x20000
	s_mov_b32 s28, s6
	s_and_b32 s29, s7, 0xffff
	s_mov_b32 s30, 0xc35000
	s_mov_b32 s31, 0x20000
	v_lshlrev_b32_e32 v238, 4, v1
	v_mul_u32_u24_e32 v253, 0x1746, v1
	v_lshrrev_b32_e32 v253, 16, v253
	v_min_u32_e32 v253, 3, v253
	v_mul_u32_u24_e32 v254, 11, v253
	v_sub_u32_e32 v254, v1, v254
	v_lshlrev_b32_e32 v240, 3, v253
	v_mul_u32_u24_e32 v249, 0x4b0, v253
	v_lshl_add_u32 v249, v254, 4, v249
	v_add_u32_e32 v249, 0x400, v249
	v_mov_b32_e32 v255, 0x80000000
	v_cmp_gt_u32_e64 s[34:35], 44, v1
	s_nop 1
	v_cndmask_b32_e64 v239, v255, v249, s[34:35]
	v_lshl_add_u32 v250, s8, 2, v253
	v_mul_u32_u24_e32 v250, 0x4e0, v250
	v_lshl_add_u32 v250, v254, 3, v250
	v_add_u32_e32 v242, 0x200, v250
	s_mul_i32 s18, s8, 0x1380
	v_lshl_add_u32 v241, v1, 3, s18
	v_and_b32_e32 v249, 15, v1
	v_lshrrev_b32_e32 v250, 4, v1
	v_mul_u32_u24_e32 v243, 0x4e0, v249
	v_lshl_add_u32 v243, v250, 4, v243
	v_mul_u32_u24_e32 v244, 0x440, v250
	v_lshl_add_u32 v244, v249, 1, v244
	s_lshl_b32 s18, s8, 6
	s_add_i32 s18, s18, 39936
	v_add_u32_e32 v244, s18, v244
	v_lshrrev_b32_e32 v249, 4, v0
	v_and_b32_e32 v250, 15, v0
	v_mul_u32_u24_e32 v245, 0x110, v249
	v_lshl_add_u32 v245, v250, 4, v245
	v_add_u32_e32 v245, 39936, v245
	v_lshlrev_b32_e32 v246, 8, v249
	v_lshl_add_u32 v246, v250, 4, v246
	s_lshl_b32 s18, s8, 12
	s_add_i32 s18, s18, 48640
	v_lshl_add_u32 v248, v1, 4, s18
	v_cmp_gt_u32_e32 vcc, 32, v0
	s_and_saveexec_b64 s[36:37], vcc
	v_mul_u32_u24_e32 v251, 0x4e00, v249
	v_mul_u32_u24_e32 v252, 0x4e0, v250
	v_add_u32_e32 v254, v251, v252
	v_mov_b32_e32 v250, 0
	v_mov_b32_e32 v251, 0
	v_mov_b32_e32 v252, 0
	v_mov_b32_e32 v253, 0
	ds_write_b128 v254, v[250:253] offset:1200
	s_mov_b64 exec, s[36:37]
	s_lshl_b32 s18, s8, 11
	v_lshl_add_u32 v253, v1, 4, s18
	v_add_u32_e32 v254, 0x22000, v253
	global_load_dwordx4 v[178:181], v254, s[4:5]
	global_load_dwordx4 v[182:185], v254, s[4:5] offset:1024
	v_add_u32_e32 v254, 0x2000, v254
	global_load_dwordx4 v[186:189], v254, s[4:5]
	global_load_dwordx4 v[190:193], v254, s[4:5] offset:1024
	v_mov_b32_e32 v236, v253
	s_waitcnt vmcnt(4)
	v_readlane_b32 s13, v247, s10
	s_add_u32 s14, s12, 0x4b0
	s_add_u32 s15, s12, 0x960
	s_add_u32 s16, s12, 0xe10
	s_nop 1
	s_and_b32 s18, s13, 0xff
	s_cmp_eq_u32 s18, 1
	s_cselect_b32 s42, s12, 0x80000000
	s_and_b32 s18, s13, 0xff00
	s_cmp_eq_u32 s18, 0x100
	s_cselect_b32 s14, s14, 0x80000000
	s_and_b32 s18, s13, 0xff0000
	s_cmp_eq_u32 s18, 0x10000
	s_cselect_b32 s15, s15, 0x80000000
	s_and_b32 s18, s13, 0xff000000
	s_cmp_eq_u32 s18, 0x1000000
	s_cselect_b32 s16, s16, 0x80000000
	v_lshrrev_b32_e64 v249, v240, s13
	v_and_b32_e32 v249, 0xff, v249
	v_cmp_eq_u32_e32 vcc, 1, v249
	s_nop 1
	v_cndmask_b32_e32 v254, v255, v239, vcc
	buffer_load_dwordx4 v[170:173], v254, s[20:23], s12 offen sc1 nt
	buffer_load_dwordx4 v[174:177], v254, s[24:27], s12 offen sc1 nt
	buffer_load_dwordx4 v[138:141], v238, s[20:23], s42 offen sc1 nt
	buffer_load_dwordx4 v[142:145], v238, s[24:27], s42 offen sc1 nt
	buffer_load_dwordx4 v[146:149], v238, s[20:23], s14 offen sc1 nt
	buffer_load_dwordx4 v[150:153], v238, s[24:27], s14 offen sc1 nt
	buffer_load_dwordx4 v[154:157], v238, s[20:23], s15 offen sc1 nt
	buffer_load_dwordx4 v[158:161], v238, s[24:27], s15 offen sc1 nt
	buffer_load_dwordx4 v[162:165], v238, s[20:23], s16 offen sc1 nt
	buffer_load_dwordx4 v[166:169], v238, s[24:27], s16 offen sc1 nt
	s_add_u32 s12, s12, 0x12c000
	s_add_u32 s32, s32, 0x40000
	s_mov_b32 s19, 0x80000000
	buffer_store_dwordx4 v[226:229], v246, s[28:31], s19 offen sc0 sc1
	s_mov_b32 s10, 1
	global_load_dwordx4 v[2:5], v236, s[4:5]
	global_load_dwordx4 v[6:9], v236, s[4:5] offset:1024
	v_add_u32_e32 v236, 0x2000, v236
	global_load_dwordx4 v[10:13], v236, s[4:5]
	global_load_dwordx4 v[14:17], v236, s[4:5] offset:1024
	v_add_u32_e32 v236, 0x2000, v236
	global_load_dwordx4 v[18:21], v236, s[4:5]
	global_load_dwordx4 v[22:25], v236, s[4:5] offset:1024
	v_add_u32_e32 v236, 0x2000, v236
	global_load_dwordx4 v[26:29], v236, s[4:5]
	global_load_dwordx4 v[30:33], v236, s[4:5] offset:1024
	v_add_u32_e32 v236, 0x2000, v236
	global_load_dwordx4 v[34:37], v236, s[4:5]
	global_load_dwordx4 v[38:41], v236, s[4:5] offset:1024
	v_add_u32_e32 v236, 0x2000, v236
	global_load_dwordx4 v[42:45], v236, s[4:5]
	global_load_dwordx4 v[46:49], v236, s[4:5] offset:1024
	v_add_u32_e32 v236, 0x2000, v236
	global_load_dwordx4 v[50:53], v236, s[4:5]
	global_load_dwordx4 v[54:57], v236, s[4:5] offset:1024
	v_add_u32_e32 v236, 0x2000, v236
	global_load_dwordx4 v[58:61], v236, s[4:5]
	global_load_dwordx4 v[62:65], v236, s[4:5] offset:1024
	v_add_u32_e32 v236, 0x2000, v236
	global_load_dwordx4 v[66:69], v236, s[4:5]
	global_load_dwordx4 v[70:73], v236, s[4:5] offset:1024
	v_add_u32_e32 v236, 0x2000, v236
	global_load_dwordx4 v[74:77], v236, s[4:5]
	global_load_dwordx4 v[78:81], v236, s[4:5] offset:1024
	v_add_u32_e32 v236, 0x2000, v236
	global_load_dwordx4 v[82:85], v236, s[4:5]
	global_load_dwordx4 v[86:89], v236, s[4:5] offset:1024
	v_add_u32_e32 v236, 0x2000, v236
	global_load_dwordx4 v[90:93], v236, s[4:5]
	global_load_dwordx4 v[94:97], v236, s[4:5] offset:1024
	v_add_u32_e32 v236, 0x2000, v236
	global_load_dwordx4 v[98:101], v236, s[4:5]
	global_load_dwordx4 v[102:105], v236, s[4:5] offset:1024
	v_add_u32_e32 v236, 0x2000, v236
	global_load_dwordx4 v[106:109], v236, s[4:5]
	global_load_dwordx4 v[110:113], v236, s[4:5] offset:1024
	v_add_u32_e32 v236, 0x2000, v236
	global_load_dwordx4 v[114:117], v236, s[4:5]
	global_load_dwordx4 v[118:121], v236, s[4:5] offset:1024
	v_add_u32_e32 v236, 0x2000, v236
	global_load_dwordx4 v[122:125], v236, s[4:5]
	global_load_dwordx4 v[126:129], v236, s[4:5] offset:1024
	v_add_u32_e32 v236, 0x2000, v236
	global_load_dwordx4 v[130:133], v236, s[4:5]
	global_load_dwordx4 v[134:137], v236, s[4:5] offset:1024
	s_waitcnt vmcnt(45)
	ds_write_b128 v248, v[178:181]
	ds_write_b128 v248, v[182:185] offset:1024
	ds_write_b128 v248, v[186:189] offset:2048
	ds_write_b128 v248, v[190:193] offset:3072
	s_waitcnt lgkmcnt(0)
	s_barrier
	s_branch .Lg_half1

.Lg_noprep0:
	s_sub_u32 s18, s10, 2
	s_cmp_lt_u32 s18, s9
	s_cbranch_scc0 .Lg_s2skip0
	s_cmp_gt_u32 s10, s9
	s_cbranch_scc1 .Lg_s2finalb0
	s_cmp_eq_u32 s10, s9
	s_cbranch_scc1 .Lg_s2final0
	s_mov_b64 exec, s[34:35]
	s_waitcnt vmcnt(21)
	v_cvt_pk_f16_f32 v250, v170, v171
	v_cvt_pk_f16_f32 v251, v172, v173
	ds_write_b64 v242, v[250:251] offset:0
	s_mov_b64 exec, -1
	buffer_load_dwordx4 v[170:173], v254, s[20:23], s12 offen sc1 nt
	s_mov_b64 exec, s[34:35]
	s_waitcnt vmcnt(21)
	v_cvt_pk_f16_f32 v252, v174, v175
	v_cvt_pk_f16_f32 v253, v176, v177
	ds_write_b64 v242, v[252:253] offset:600
	s_mov_b64 exec, -1
	buffer_load_dwordx4 v[174:177], v254, s[24:27], s12 offen sc1 nt
	s_waitcnt vmcnt(21)
	v_cvt_pk_f16_f32 v250, v138, v139
	v_cvt_pk_f16_f32 v251, v140, v141
	ds_write_b64 v241, v[250:251] offset:0
	buffer_load_dwordx4 v[138:141], v238, s[20:23], s42 offen sc1 nt
	s_waitcnt vmcnt(21)
	v_cvt_pk_f16_f32 v252, v142, v143
	v_cvt_pk_f16_f32 v253, v144, v145
	ds_write_b64 v241, v[252:253] offset:600
	buffer_load_dwordx4 v[142:145], v238, s[24:27], s42 offen sc1 nt
	s_waitcnt vmcnt(21)
	v_cvt_pk_f16_f32 v250, v146, v147
	v_cvt_pk_f16_f32 v251, v148, v149
	ds_write_b64 v241, v[250:251] offset:1248
	buffer_load_dwordx4 v[146:149], v238, s[20:23], s14 offen sc1 nt
	s_waitcnt vmcnt(21)
	v_cvt_pk_f16_f32 v252, v150, v151
	v_cvt_pk_f16_f32 v253, v152, v153
	ds_write_b64 v241, v[252:253] offset:1848
	buffer_load_dwordx4 v[150:153], v238, s[24:27], s14 offen sc1 nt
	s_waitcnt vmcnt(21)
	v_cvt_pk_f16_f32 v250, v154, v155
	v_cvt_pk_f16_f32 v251, v156, v157
	ds_write_b64 v241, v[250:251] offset:2496
	buffer_load_dwordx4 v[154:157], v238, s[20:23], s15 offen sc1 nt
	s_waitcnt vmcnt(21)
	v_cvt_pk_f16_f32 v252, v158, v159
	v_cvt_pk_f16_f32 v253, v160, v161
	ds_write_b64 v241, v[252:253] offset:3096
	buffer_load_dwordx4 v[158:161], v238, s[24:27], s15 offen sc1 nt
	s_waitcnt vmcnt(21)
	v_cvt_pk_f16_f32 v250, v162, v163
	v_cvt_pk_f16_f32 v251, v164, v165
	ds_write_b64 v241, v[250:251] offset:3744
	buffer_load_dwordx4 v[162:165], v238, s[20:23], s16 offen sc1 nt
	s_waitcnt vmcnt(21)
	v_cvt_pk_f16_f32 v252, v166, v167
	v_cvt_pk_f16_f32 v253, v168, v169
	ds_write_b64 v241, v[252:253] offset:4344
	buffer_load_dwordx4 v[166:169], v238, s[24:27], s16 offen sc1 nt
	s_branch .Lg_s1done0
.Lg_s2final0:
	s_mov_b64 exec, s[34:35]
	s_waitcnt vmcnt(21)
	v_cvt_pk_f16_f32 v250, v170, v171
	v_cvt_pk_f16_f32 v251, v172, v173
	ds_write_b64 v242, v[250:251] offset:0
	s_mov_b64 exec, -1
	s_mov_b64 exec, s[34:35]
	s_waitcnt vmcnt(20)
	v_cvt_pk_f16_f32 v252, v174, v175
	v_cvt_pk_f16_f32 v253, v176, v177
	ds_write_b64 v242, v[252:253] offset:600
	s_mov_b64 exec, -1
	s_waitcnt vmcnt(19)
	v_cvt_pk_f16_f32 v250, v138, v139
	v_cvt_pk_f16_f32 v251, v140, v141
	ds_write_b64 v241, v[250:251] offset:0
	s_waitcnt vmcnt(18)
	v_cvt_pk_f16_f32 v252, v142, v143
	v_cvt_pk_f16_f32 v253, v144, v145
	ds_write_b64 v241, v[252:253] offset:600
	s_waitcnt vmcnt(17)
	v_cvt_pk_f16_f32 v250, v146, v147
	v_cvt_pk_f16_f32 v251, v148, v149
	ds_write_b64 v241, v[250:251] offset:1248
	s_waitcnt vmcnt(16)
	v_cvt_pk_f16_f32 v252, v150, v151
	v_cvt_pk_f16_f32 v253, v152, v153
	ds_write_b64 v241, v[252:253] offset:1848
	s_waitcnt vmcnt(15)
	v_cvt_pk_f16_f32 v250, v154, v155
	v_cvt_pk_f16_f32 v251, v156, v157
	ds_write_b64 v241, v[250:251] offset:2496
	s_waitcnt vmcnt(14)
	v_cvt_pk_f16_f32 v252, v158, v159
	v_cvt_pk_f16_f32 v253, v160, v161
	ds_write_b64 v241, v[252:253] offset:3096
	s_waitcnt vmcnt(13)
	v_cvt_pk_f16_f32 v250, v162, v163
	v_cvt_pk_f16_f32 v251, v164, v165
	ds_write_b64 v241, v[250:251] offset:3744
	s_waitcnt vmcnt(12)
	v_cvt_pk_f16_f32 v252, v166, v167
	v_cvt_pk_f16_f32 v253, v168, v169
	ds_write_b64 v241, v[252:253] offset:4344
	s_branch .Lg_s1done0
.Lg_s2finalb0:
	s_mov_b64 exec, s[34:35]
	s_waitcnt vmcnt(11)
	v_cvt_pk_f16_f32 v250, v170, v171
	v_cvt_pk_f16_f32 v251, v172, v173
	ds_write_b64 v242, v[250:251] offset:0
	s_mov_b64 exec, -1
	s_mov_b64 exec, s[34:35]
	s_waitcnt vmcnt(10)
	v_cvt_pk_f16_f32 v252, v174, v175
	v_cvt_pk_f16_f32 v253, v176, v177
	ds_write_b64 v242, v[252:253] offset:600
	s_mov_b64 exec, -1
	s_waitcnt vmcnt(9)
	v_cvt_pk_f16_f32 v250, v138, v139
	v_cvt_pk_f16_f32 v251, v140, v141
	ds_write_b64 v241, v[250:251] offset:0
	s_waitcnt vmcnt(8)
	v_cvt_pk_f16_f32 v252, v142, v143
	v_cvt_pk_f16_f32 v253, v144, v145
	ds_write_b64 v241, v[252:253] offset:600
	s_waitcnt vmcnt(7)
	v_cvt_pk_f16_f32 v250, v146, v147
	v_cvt_pk_f16_f32 v251, v148, v149
	ds_write_b64 v241, v[250:251] offset:1248
	s_waitcnt vmcnt(6)
	v_cvt_pk_f16_f32 v252, v150, v151
	v_cvt_pk_f16_f32 v253, v152, v153
	ds_write_b64 v241, v[252:253] offset:1848
	s_waitcnt vmcnt(5)
	v_cvt_pk_f16_f32 v250, v154, v155
	v_cvt_pk_f16_f32 v251, v156, v157
	ds_write_b64 v241, v[250:251] offset:2496
	s_waitcnt vmcnt(4)
	v_cvt_pk_f16_f32 v252, v158, v159
	v_cvt_pk_f16_f32 v253, v160, v161
	ds_write_b64 v241, v[252:253] offset:3096
	s_waitcnt vmcnt(3)
	v_cvt_pk_f16_f32 v250, v162, v163
	v_cvt_pk_f16_f32 v251, v164, v165
	ds_write_b64 v241, v[250:251] offset:3744
	s_waitcnt vmcnt(2)
	v_cvt_pk_f16_f32 v252, v166, v167
	v_cvt_pk_f16_f32 v253, v168, v169
	ds_write_b64 v241, v[252:253] offset:4344
	s_branch .Lg_s1done0
.Lg_s2skip0:
	s_cmp_ge_u32 s10, s9
	s_cbranch_scc1 .Lg_s1done0
	buffer_load_dwordx4 v[170:173], v254, s[20:23], s12 offen sc1 nt
	buffer_load_dwordx4 v[174:177], v254, s[24:27], s12 offen sc1 nt
	buffer_load_dwordx4 v[138:141], v238, s[20:23], s42 offen sc1 nt
	buffer_load_dwordx4 v[142:145], v238, s[24:27], s42 offen sc1 nt
	buffer_load_dwordx4 v[146:149], v238, s[20:23], s14 offen sc1 nt
	buffer_load_dwordx4 v[150:153], v238, s[24:27], s14 offen sc1 nt
	buffer_load_dwordx4 v[154:157], v238, s[20:23], s15 offen sc1 nt
	buffer_load_dwordx4 v[158:161], v238, s[24:27], s15 offen sc1 nt
	buffer_load_dwordx4 v[162:165], v238, s[20:23], s16 offen sc1 nt
	buffer_load_dwordx4 v[166:169], v238, s[24:27], s16 offen sc1 nt

.Lg_noprep1:
	s_sub_u32 s18, s10, 2
	s_cmp_lt_u32 s18, s9
	s_cbranch_scc0 .Lg_s2skip1
	s_cmp_gt_u32 s10, s9
	s_cbranch_scc1 .Lg_s2finalb1
	s_cmp_eq_u32 s10, s9
	s_cbranch_scc1 .Lg_s2final1
	s_mov_b64 exec, s[34:35]
	s_waitcnt vmcnt(21)
	v_cvt_pk_f16_f32 v250, v210, v211
	v_cvt_pk_f16_f32 v251, v212, v213
	ds_write_b64 v242, v[250:251] offset:19968
	s_mov_b64 exec, -1
	buffer_load_dwordx4 v[210:213], v254, s[20:23], s12 offen sc1 nt
	s_mov_b64 exec, s[34:35]
	s_waitcnt vmcnt(21)
	v_cvt_pk_f16_f32 v252, v214, v215
	v_cvt_pk_f16_f32 v253, v216, v217
	ds_write_b64 v242, v[252:253] offset:20568
	s_mov_b64 exec, -1
	buffer_load_dwordx4 v[214:217], v254, s[24:27], s12 offen sc1 nt
	s_waitcnt vmcnt(21)
	v_cvt_pk_f16_f32 v250, v178, v179
	v_cvt_pk_f16_f32 v251, v180, v181
	ds_write_b64 v241, v[250:251] offset:19968
	buffer_load_dwordx4 v[178:181], v238, s[20:23], s42 offen sc1 nt
	s_waitcnt vmcnt(21)
	v_cvt_pk_f16_f32 v252, v182, v183
	v_cvt_pk_f16_f32 v253, v184, v185
	ds_write_b64 v241, v[252:253] offset:20568
	buffer_load_dwordx4 v[182:185], v238, s[24:27], s42 offen sc1 nt
	s_waitcnt vmcnt(21)
	v_cvt_pk_f16_f32 v250, v186, v187
	v_cvt_pk_f16_f32 v251, v188, v189
	ds_write_b64 v241, v[250:251] offset:21216
	buffer_load_dwordx4 v[186:189], v238, s[20:23], s14 offen sc1 nt
	s_waitcnt vmcnt(21)
	v_cvt_pk_f16_f32 v252, v190, v191
	v_cvt_pk_f16_f32 v253, v192, v193
	ds_write_b64 v241, v[252:253] offset:21816
	buffer_load_dwordx4 v[190:193], v238, s[24:27], s14 offen sc1 nt
	s_waitcnt vmcnt(21)
	v_cvt_pk_f16_f32 v250, v194, v195
	v_cvt_pk_f16_f32 v251, v196, v197
	ds_write_b64 v241, v[250:251] offset:22464
	buffer_load_dwordx4 v[194:197], v238, s[20:23], s15 offen sc1 nt
	s_waitcnt vmcnt(21)
	v_cvt_pk_f16_f32 v252, v198, v199
	v_cvt_pk_f16_f32 v253, v200, v201
	ds_write_b64 v241, v[252:253] offset:23064
	buffer_load_dwordx4 v[198:201], v238, s[24:27], s15 offen sc1 nt
	s_waitcnt vmcnt(21)
	v_cvt_pk_f16_f32 v250, v202, v203
	v_cvt_pk_f16_f32 v251, v204, v205
	ds_write_b64 v241, v[250:251] offset:23712
	buffer_load_dwordx4 v[202:205], v238, s[20:23], s16 offen sc1 nt
	s_waitcnt vmcnt(21)
	v_cvt_pk_f16_f32 v252, v206, v207
	v_cvt_pk_f16_f32 v253, v208, v209
	ds_write_b64 v241, v[252:253] offset:24312
	buffer_load_dwordx4 v[206:209], v238, s[24:27], s16 offen sc1 nt
	s_branch .Lg_s1done1
.Lg_s2final1:
	s_mov_b64 exec, s[34:35]
	s_waitcnt vmcnt(21)
	v_cvt_pk_f16_f32 v250, v210, v211
	v_cvt_pk_f16_f32 v251, v212, v213
	ds_write_b64 v242, v[250:251] offset:19968
	s_mov_b64 exec, -1
	s_mov_b64 exec, s[34:35]
	s_waitcnt vmcnt(20)
	v_cvt_pk_f16_f32 v252, v214, v215
	v_cvt_pk_f16_f32 v253, v216, v217
	ds_write_b64 v242, v[252:253] offset:20568
	s_mov_b64 exec, -1
	s_waitcnt vmcnt(19)
	v_cvt_pk_f16_f32 v250, v178, v179
	v_cvt_pk_f16_f32 v251, v180, v181
	ds_write_b64 v241, v[250:251] offset:19968
	s_waitcnt vmcnt(18)
	v_cvt_pk_f16_f32 v252, v182, v183
	v_cvt_pk_f16_f32 v253, v184, v185
	ds_write_b64 v241, v[252:253] offset:20568
	s_waitcnt vmcnt(17)
	v_cvt_pk_f16_f32 v250, v186, v187
	v_cvt_pk_f16_f32 v251, v188, v189
	ds_write_b64 v241, v[250:251] offset:21216
	s_waitcnt vmcnt(16)
	v_cvt_pk_f16_f32 v252, v190, v191
	v_cvt_pk_f16_f32 v253, v192, v193
	ds_write_b64 v241, v[252:253] offset:21816
	s_waitcnt vmcnt(15)
	v_cvt_pk_f16_f32 v250, v194, v195
	v_cvt_pk_f16_f32 v251, v196, v197
	ds_write_b64 v241, v[250:251] offset:22464
	s_waitcnt vmcnt(14)
	v_cvt_pk_f16_f32 v252, v198, v199
	v_cvt_pk_f16_f32 v253, v200, v201
	ds_write_b64 v241, v[252:253] offset:23064
	s_waitcnt vmcnt(13)
	v_cvt_pk_f16_f32 v250, v202, v203
	v_cvt_pk_f16_f32 v251, v204, v205
	ds_write_b64 v241, v[250:251] offset:23712
	s_waitcnt vmcnt(12)
	v_cvt_pk_f16_f32 v252, v206, v207
	v_cvt_pk_f16_f32 v253, v208, v209
	ds_write_b64 v241, v[252:253] offset:24312
	s_branch .Lg_s1done1
.Lg_s2finalb1:
	s_mov_b64 exec, s[34:35]
	s_waitcnt vmcnt(11)
	v_cvt_pk_f16_f32 v250, v210, v211
	v_cvt_pk_f16_f32 v251, v212, v213
	ds_write_b64 v242, v[250:251] offset:19968
	s_mov_b64 exec, -1
	s_mov_b64 exec, s[34:35]
	s_waitcnt vmcnt(10)
	v_cvt_pk_f16_f32 v252, v214, v215
	v_cvt_pk_f16_f32 v253, v216, v217
	ds_write_b64 v242, v[252:253] offset:20568
	s_mov_b64 exec, -1
	s_waitcnt vmcnt(9)
	v_cvt_pk_f16_f32 v250, v178, v179
	v_cvt_pk_f16_f32 v251, v180, v181
	ds_write_b64 v241, v[250:251] offset:19968
	s_waitcnt vmcnt(8)
	v_cvt_pk_f16_f32 v252, v182, v183
	v_cvt_pk_f16_f32 v253, v184, v185
	ds_write_b64 v241, v[252:253] offset:20568
	s_waitcnt vmcnt(7)
	v_cvt_pk_f16_f32 v250, v186, v187
	v_cvt_pk_f16_f32 v251, v188, v189
	ds_write_b64 v241, v[250:251] offset:21216
	s_waitcnt vmcnt(6)
	v_cvt_pk_f16_f32 v252, v190, v191
	v_cvt_pk_f16_f32 v253, v192, v193
	ds_write_b64 v241, v[252:253] offset:21816
	s_waitcnt vmcnt(5)
	v_cvt_pk_f16_f32 v250, v194, v195
	v_cvt_pk_f16_f32 v251, v196, v197
	ds_write_b64 v241, v[250:251] offset:22464
	s_waitcnt vmcnt(4)
	v_cvt_pk_f16_f32 v252, v198, v199
	v_cvt_pk_f16_f32 v253, v200, v201
	ds_write_b64 v241, v[252:253] offset:23064
	s_waitcnt vmcnt(3)
	v_cvt_pk_f16_f32 v250, v202, v203
	v_cvt_pk_f16_f32 v251, v204, v205
	ds_write_b64 v241, v[250:251] offset:23712
	s_waitcnt vmcnt(2)
	v_cvt_pk_f16_f32 v252, v206, v207
	v_cvt_pk_f16_f32 v253, v208, v209
	ds_write_b64 v241, v[252:253] offset:24312
	s_branch .Lg_s1done1
.Lg_s2skip1:
	s_cmp_ge_u32 s10, s9
	s_cbranch_scc1 .Lg_s1done1
	buffer_load_dwordx4 v[210:213], v254, s[20:23], s12 offen sc1 nt
	buffer_load_dwordx4 v[214:217], v254, s[24:27], s12 offen sc1 nt
	buffer_load_dwordx4 v[178:181], v238, s[20:23], s42 offen sc1 nt
	buffer_load_dwordx4 v[182:185], v238, s[24:27], s42 offen sc1 nt
	buffer_load_dwordx4 v[186:189], v238, s[20:23], s14 offen sc1 nt
	buffer_load_dwordx4 v[190:193], v238, s[24:27], s14 offen sc1 nt
	buffer_load_dwordx4 v[194:197], v238, s[20:23], s15 offen sc1 nt
	buffer_load_dwordx4 v[198:201], v238, s[24:27], s15 offen sc1 nt
	buffer_load_dwordx4 v[202:205], v238, s[20:23], s16 offen sc1 nt
	buffer_load_dwordx4 v[206:209], v238, s[24:27], s16 offen sc1 nt
